# speedup vs baseline: 1.0039x; 1.0039x over previous
.LBB3_11:
	s_lshl_b32 s58, s42, 7
	s_add_i32 s59, s41, 0x400
	s_lshr_b32 s59, s59, 6
	s_bfe_u32 s60, s20, 0x1000c
	s_add_i32 s59, s59, s60
	s_lshl_b32 s59, s59, 19
	s_add_u32 s58, s58, s59
	s_add_u32 s58, s56, s58
	s_addc_u32 s59, s57, 0
	s_add_u32 s60, s58, 0x4000
	s_addc_u32 s61, s59, 0
	s_add_u32 s62, s58, 0x100000
	s_addc_u32 s63, s59, 0
	s_add_u32 s64, s62, 0x4000
	s_addc_u32 s65, s63, 0
	s_lshr_b32 s66, s41, 7
	s_bfe_u32 s67, s20, 0x1000c
	s_add_i32 s66, s66, s67
	s_lshl_b32 s66, s66, 14
	s_lshl_b32 s67, s42, 2
	s_add_u32 s66, s66, s67
	s_add_u32 s66, s14, s66
	s_addc_u32 s67, s15, 0
	v_add_u32_e32 v172, s43, v207
	v_exp_f32_e32 v130, v114
	v_exp_f32_e32 v131, v115
	v_exp_f32_e32 v132, v116
	v_exp_f32_e32 v133, v117
	v_exp_f32_e32 v142, v78
	v_exp_f32_e32 v143, v79
	v_exp_f32_e32 v144, v80
	v_exp_f32_e32 v145, v81
	v_exp_f32_e32 v176, v106
	v_exp_f32_e32 v177, v107
	v_exp_f32_e32 v178, v108
	v_exp_f32_e32 v179, v109
	v_exp_f32_e32 v232, v70
	v_exp_f32_e32 v233, v71
	v_exp_f32_e32 v234, v72
	v_exp_f32_e32 v235, v73
	v_pk_fma_f32 v[130:131], v[130:131], -0.5, -0.5 op_sel_hi:[1,0,0]
	v_pk_fma_f32 v[132:133], v[132:133], -0.5, -0.5 op_sel_hi:[1,0,0]
	v_pk_fma_f32 v[142:143], v[142:143], -0.5, -0.5 op_sel_hi:[1,0,0]
	v_pk_fma_f32 v[144:145], v[144:145], -0.5, -0.5 op_sel_hi:[1,0,0]
	v_pk_fma_f32 v[176:177], v[176:177], -0.5, -0.5 op_sel_hi:[1,0,0]
	v_pk_fma_f32 v[178:179], v[178:179], -0.5, -0.5 op_sel_hi:[1,0,0]
	v_pk_fma_f32 v[232:233], v[232:233], -0.5, -0.5 op_sel_hi:[1,0,0]
	v_pk_fma_f32 v[234:235], v[234:235], -0.5, -0.5 op_sel_hi:[1,0,0]
	v_pk_mul_f32 v[134:135], v[130:131], v[132:133]
	v_pk_mul_f32 v[146:147], v[142:143], v[144:145]
	v_pk_mul_f32 v[180:181], v[176:177], v[178:179]
	v_pk_mul_f32 v[236:237], v[232:233], v[234:235]
	v_mul_f32_e32 v138, v134, v135
	v_mul_f32_e32 v150, v146, v147
	v_mul_f32_e32 v184, v180, v181
	v_mul_f32_e32 v240, v236, v237
	v_rcp_f32_e32 v138, v138
	v_rcp_f32_e32 v150, v150
	v_rcp_f32_e32 v184, v184
	v_rcp_f32_e32 v240, v240
	v_pk_add_f32 v[164:165], v[114:115], v[116:117]
	v_pk_add_f32 v[164:165], v[164:165], v[78:79]
	v_pk_add_f32 v[164:165], v[164:165], v[80:81]
	v_pk_add_f32 v[164:165], v[164:165], v[106:107]
	v_pk_add_f32 v[164:165], v[164:165], v[108:109]
	v_pk_add_f32 v[164:165], v[164:165], v[70:71]
	v_pk_add_f32 v[164:165], v[164:165], v[72:73]
	v_pk_mul_f32 v[162:163], v[134:135], v[146:147]
	v_pk_mul_f32 v[162:163], v[162:163], v[180:181]
	v_pk_mul_f32 v[162:163], v[162:163], v[236:237]
	v_pk_mul_f32 v[136:137], v[138:139], v[134:135] op_sel:[0,1] op_sel_hi:[0,0]
	v_pk_mul_f32 v[148:149], v[150:151], v[146:147] op_sel:[0,1] op_sel_hi:[0,0]
	v_pk_mul_f32 v[182:183], v[184:185], v[180:181] op_sel:[0,1] op_sel_hi:[0,0]
	v_pk_mul_f32 v[238:239], v[240:241], v[236:237] op_sel:[0,1] op_sel_hi:[0,0]
	v_pk_fma_f32 v[138:139], v[136:137], v[132:133], 1.0 op_sel_hi:[1,1,0]
	v_pk_fma_f32 v[140:141], v[136:137], v[130:131], 1.0 op_sel_hi:[1,1,0]
	v_pk_fma_f32 v[150:151], v[148:149], v[144:145], 1.0 op_sel_hi:[1,1,0]
	v_pk_fma_f32 v[152:153], v[148:149], v[142:143], 1.0 op_sel_hi:[1,1,0]
	v_pk_fma_f32 v[184:185], v[182:183], v[178:179], 1.0 op_sel_hi:[1,1,0]
	v_pk_fma_f32 v[186:187], v[182:183], v[176:177], 1.0 op_sel_hi:[1,1,0]
	v_pk_fma_f32 v[240:241], v[238:239], v[234:235], 1.0 op_sel_hi:[1,1,0]
	v_pk_fma_f32 v[242:243], v[238:239], v[232:233], 1.0 op_sel_hi:[1,1,0]
	v_cvt_pk_bf16_f32 v154, v138, v139
	v_cvt_pk_bf16_f32 v155, v140, v141
	v_cvt_pk_bf16_f32 v156, v150, v151
	v_cvt_pk_bf16_f32 v157, v152, v153
	v_cvt_pk_bf16_f32 v158, v184, v185
	v_cvt_pk_bf16_f32 v159, v186, v187
	v_cvt_pk_bf16_f32 v160, v240, v241
	v_cvt_pk_bf16_f32 v161, v242, v243
	ds_read_b128 v[114:117], v172
	ds_read_b128 v[78:81], v172 offset:64
	ds_read_b128 v[106:109], v172 offset:128
	ds_read_b128 v[70:73], v172 offset:192
	v_permlane16_swap_b32_e32 v154, v156
	v_permlane16_swap_b32_e32 v155, v157
	global_store_dwordx4 v228, v[154:157], s[58:59] nt
	s_bitcmp1_b32 s20, 12
	s_cbranch_scc1 .Lg1_noX
	s_barrier
.Lg1_noX:
	v_permlane16_swap_b32_e32 v158, v160
	v_permlane16_swap_b32_e32 v159, v161
	global_store_dwordx4 v228, v[158:161], s[58:59] offset:128 nt
	v_exp_f32_e32 v130, v90
	v_exp_f32_e32 v131, v91
	v_exp_f32_e32 v132, v92
	v_exp_f32_e32 v133, v93
	v_exp_f32_e32 v142, v42
	v_exp_f32_e32 v143, v43
	v_exp_f32_e32 v144, v44
	v_exp_f32_e32 v145, v45
	v_exp_f32_e32 v176, v126
	v_exp_f32_e32 v177, v127
	v_exp_f32_e32 v178, v128
	v_exp_f32_e32 v179, v129
	v_exp_f32_e32 v232, v58
	v_exp_f32_e32 v233, v59
	v_exp_f32_e32 v234, v60
	v_exp_f32_e32 v235, v61
	v_pk_fma_f32 v[130:131], v[130:131], -0.5, -0.5 op_sel_hi:[1,0,0]
	v_pk_fma_f32 v[132:133], v[132:133], -0.5, -0.5 op_sel_hi:[1,0,0]
	v_pk_fma_f32 v[142:143], v[142:143], -0.5, -0.5 op_sel_hi:[1,0,0]
	v_pk_fma_f32 v[144:145], v[144:145], -0.5, -0.5 op_sel_hi:[1,0,0]
	v_pk_fma_f32 v[176:177], v[176:177], -0.5, -0.5 op_sel_hi:[1,0,0]
	v_pk_fma_f32 v[178:179], v[178:179], -0.5, -0.5 op_sel_hi:[1,0,0]
	v_pk_fma_f32 v[232:233], v[232:233], -0.5, -0.5 op_sel_hi:[1,0,0]
	v_pk_fma_f32 v[234:235], v[234:235], -0.5, -0.5 op_sel_hi:[1,0,0]
	v_pk_mul_f32 v[134:135], v[130:131], v[132:133]
	v_pk_mul_f32 v[146:147], v[142:143], v[144:145]
	v_pk_mul_f32 v[180:181], v[176:177], v[178:179]
	v_pk_mul_f32 v[236:237], v[232:233], v[234:235]
	v_mul_f32_e32 v138, v134, v135
	v_mul_f32_e32 v150, v146, v147
	v_mul_f32_e32 v184, v180, v181
	v_mul_f32_e32 v240, v236, v237
	v_rcp_f32_e32 v138, v138
	v_rcp_f32_e32 v150, v150
	v_rcp_f32_e32 v184, v184
	v_rcp_f32_e32 v240, v240
	v_pk_add_f32 v[164:165], v[164:165], v[90:91]
	v_pk_add_f32 v[164:165], v[164:165], v[92:93]
	v_pk_add_f32 v[164:165], v[164:165], v[42:43]
	v_pk_add_f32 v[164:165], v[164:165], v[44:45]
	v_pk_add_f32 v[164:165], v[164:165], v[126:127]
	v_pk_add_f32 v[164:165], v[164:165], v[128:129]
	v_pk_add_f32 v[164:165], v[164:165], v[58:59]
	v_pk_add_f32 v[164:165], v[164:165], v[60:61]
	v_pk_mul_f32 v[174:175], v[134:135], v[146:147]
	v_pk_mul_f32 v[174:175], v[174:175], v[180:181]
	v_pk_mul_f32 v[174:175], v[174:175], v[236:237]
	v_pk_mul_f32 v[136:137], v[138:139], v[134:135] op_sel:[0,1] op_sel_hi:[0,0]
	v_pk_mul_f32 v[148:149], v[150:151], v[146:147] op_sel:[0,1] op_sel_hi:[0,0]
	v_pk_mul_f32 v[182:183], v[184:185], v[180:181] op_sel:[0,1] op_sel_hi:[0,0]
	v_pk_mul_f32 v[238:239], v[240:241], v[236:237] op_sel:[0,1] op_sel_hi:[0,0]
	v_pk_fma_f32 v[138:139], v[136:137], v[132:133], 1.0 op_sel_hi:[1,1,0]
	v_pk_fma_f32 v[140:141], v[136:137], v[130:131], 1.0 op_sel_hi:[1,1,0]
	v_pk_fma_f32 v[150:151], v[148:149], v[144:145], 1.0 op_sel_hi:[1,1,0]
	v_pk_fma_f32 v[152:153], v[148:149], v[142:143], 1.0 op_sel_hi:[1,1,0]
	v_pk_fma_f32 v[184:185], v[182:183], v[178:179], 1.0 op_sel_hi:[1,1,0]
	v_pk_fma_f32 v[186:187], v[182:183], v[176:177], 1.0 op_sel_hi:[1,1,0]
	v_pk_fma_f32 v[240:241], v[238:239], v[234:235], 1.0 op_sel_hi:[1,1,0]
	v_pk_fma_f32 v[242:243], v[238:239], v[232:233], 1.0 op_sel_hi:[1,1,0]
	v_cvt_pk_bf16_f32 v154, v138, v139
	v_cvt_pk_bf16_f32 v155, v140, v141
	v_cvt_pk_bf16_f32 v156, v150, v151
	v_cvt_pk_bf16_f32 v157, v152, v153
	v_cvt_pk_bf16_f32 v158, v184, v185
	v_cvt_pk_bf16_f32 v159, v186, v187
	v_cvt_pk_bf16_f32 v160, v240, v241
	v_cvt_pk_bf16_f32 v161, v242, v243
	ds_read_b128 v[90:93], v172 offset:512
	ds_read_b128 v[42:45], v172 offset:576
	ds_read_b128 v[126:129], v172 offset:640
	ds_read_b128 v[58:61], v172 offset:704
	v_permlane16_swap_b32_e32 v154, v156
	v_permlane16_swap_b32_e32 v155, v157
	global_store_dwordx4 v228, v[154:157], s[62:63] nt
	v_permlane16_swap_b32_e32 v158, v160
	v_permlane16_swap_b32_e32 v159, v161
	global_store_dwordx4 v228, v[158:161], s[62:63] offset:128 nt
	v_log_f32_e32 v166, v162
	v_log_f32_e32 v167, v163
	v_log_f32_e32 v170, v174
	v_log_f32_e32 v171, v175
	v_add_f32_e32 v168, v164, v165
	v_mul_f32_e32 v168, 0xbeb17218, v168
	v_add_f32_e32 v166, v166, v167
	v_add_f32_e32 v170, v170, v171
	v_add_f32_e32 v166, v166, v170
	v_fmac_f32_e32 v168, 0x3f317218, v166
	v_mov_b32_e32 v169, v168
	s_nop 1
	v_permlane16_swap_b32_e32 v168, v169
	v_add_f32_e32 v168, v168, v169
	v_mov_b32_e32 v169, v168
	s_nop 1
	v_permlane32_swap_b32_e32 v168, v169
	v_add_f32_e32 v168, v168, v169
	s_mov_b64 exec, s[0:1]
	global_store_dword v229, v168, s[66:67]
	s_mov_b64 exec, -1
	v_exp_f32_e32 v130, v110
	v_exp_f32_e32 v131, v111
	v_exp_f32_e32 v132, v112
	v_exp_f32_e32 v133, v113
	v_exp_f32_e32 v142, v74
	v_exp_f32_e32 v143, v75
	v_exp_f32_e32 v144, v76
	v_exp_f32_e32 v145, v77
	v_exp_f32_e32 v176, v102
	v_exp_f32_e32 v177, v103
	v_exp_f32_e32 v178, v104
	v_exp_f32_e32 v179, v105
	v_exp_f32_e32 v232, v66
	v_exp_f32_e32 v233, v67
	v_exp_f32_e32 v234, v68
	v_exp_f32_e32 v235, v69
	v_pk_fma_f32 v[130:131], v[130:131], -0.5, -0.5 op_sel_hi:[1,0,0]
	v_pk_fma_f32 v[132:133], v[132:133], -0.5, -0.5 op_sel_hi:[1,0,0]
	v_pk_fma_f32 v[142:143], v[142:143], -0.5, -0.5 op_sel_hi:[1,0,0]
	v_pk_fma_f32 v[144:145], v[144:145], -0.5, -0.5 op_sel_hi:[1,0,0]
	v_pk_fma_f32 v[176:177], v[176:177], -0.5, -0.5 op_sel_hi:[1,0,0]
	v_pk_fma_f32 v[178:179], v[178:179], -0.5, -0.5 op_sel_hi:[1,0,0]
	v_pk_fma_f32 v[232:233], v[232:233], -0.5, -0.5 op_sel_hi:[1,0,0]
	v_pk_fma_f32 v[234:235], v[234:235], -0.5, -0.5 op_sel_hi:[1,0,0]
	v_pk_mul_f32 v[134:135], v[130:131], v[132:133]
	v_pk_mul_f32 v[146:147], v[142:143], v[144:145]
	v_pk_mul_f32 v[180:181], v[176:177], v[178:179]
	v_pk_mul_f32 v[236:237], v[232:233], v[234:235]
	v_mul_f32_e32 v138, v134, v135
	v_mul_f32_e32 v150, v146, v147
	v_mul_f32_e32 v184, v180, v181
	v_mul_f32_e32 v240, v236, v237
	v_rcp_f32_e32 v138, v138
	v_rcp_f32_e32 v150, v150
	v_rcp_f32_e32 v184, v184
	v_rcp_f32_e32 v240, v240
	v_pk_add_f32 v[164:165], v[110:111], v[112:113]
	v_pk_add_f32 v[164:165], v[164:165], v[74:75]
	v_pk_add_f32 v[164:165], v[164:165], v[76:77]
	v_pk_add_f32 v[164:165], v[164:165], v[102:103]
	v_pk_add_f32 v[164:165], v[164:165], v[104:105]
	v_pk_add_f32 v[164:165], v[164:165], v[66:67]
	v_pk_add_f32 v[164:165], v[164:165], v[68:69]
	v_pk_mul_f32 v[162:163], v[134:135], v[146:147]
	v_pk_mul_f32 v[162:163], v[162:163], v[180:181]
	v_pk_mul_f32 v[162:163], v[162:163], v[236:237]
	v_pk_mul_f32 v[136:137], v[138:139], v[134:135] op_sel:[0,1] op_sel_hi:[0,0]
	v_pk_mul_f32 v[148:149], v[150:151], v[146:147] op_sel:[0,1] op_sel_hi:[0,0]
	v_pk_mul_f32 v[182:183], v[184:185], v[180:181] op_sel:[0,1] op_sel_hi:[0,0]
	v_pk_mul_f32 v[238:239], v[240:241], v[236:237] op_sel:[0,1] op_sel_hi:[0,0]
	v_pk_fma_f32 v[138:139], v[136:137], v[132:133], 1.0 op_sel_hi:[1,1,0]
	v_pk_fma_f32 v[140:141], v[136:137], v[130:131], 1.0 op_sel_hi:[1,1,0]
	v_pk_fma_f32 v[150:151], v[148:149], v[144:145], 1.0 op_sel_hi:[1,1,0]
	v_pk_fma_f32 v[152:153], v[148:149], v[142:143], 1.0 op_sel_hi:[1,1,0]
	v_pk_fma_f32 v[184:185], v[182:183], v[178:179], 1.0 op_sel_hi:[1,1,0]
	v_pk_fma_f32 v[186:187], v[182:183], v[176:177], 1.0 op_sel_hi:[1,1,0]
	v_pk_fma_f32 v[240:241], v[238:239], v[234:235], 1.0 op_sel_hi:[1,1,0]
	v_pk_fma_f32 v[242:243], v[238:239], v[232:233], 1.0 op_sel_hi:[1,1,0]
	v_cvt_pk_bf16_f32 v154, v138, v139
	v_cvt_pk_bf16_f32 v155, v140, v141
	v_cvt_pk_bf16_f32 v156, v150, v151
	v_cvt_pk_bf16_f32 v157, v152, v153
	v_cvt_pk_bf16_f32 v158, v184, v185
	v_cvt_pk_bf16_f32 v159, v186, v187
	v_cvt_pk_bf16_f32 v160, v240, v241
	v_cvt_pk_bf16_f32 v161, v242, v243
	ds_read_b128 v[110:113], v172
	ds_read_b128 v[74:77], v172 offset:64
	ds_read_b128 v[102:105], v172 offset:128
	ds_read_b128 v[66:69], v172 offset:192
	v_permlane16_swap_b32_e32 v154, v156
	v_permlane16_swap_b32_e32 v155, v157
	global_store_dwordx4 v228, v[154:157], s[58:59] offset:2048 nt
	v_permlane16_swap_b32_e32 v158, v160
	v_permlane16_swap_b32_e32 v159, v161
	global_store_dwordx4 v228, v[158:161], s[58:59] offset:2176 nt
	v_exp_f32_e32 v130, v86
	v_exp_f32_e32 v131, v87
	v_exp_f32_e32 v132, v88
	v_exp_f32_e32 v133, v89
	v_exp_f32_e32 v142, v38
	v_exp_f32_e32 v143, v39
	v_exp_f32_e32 v144, v40
	v_exp_f32_e32 v145, v41
	v_exp_f32_e32 v176, v122
	v_exp_f32_e32 v177, v123
	v_exp_f32_e32 v178, v124
	v_exp_f32_e32 v179, v125
	v_exp_f32_e32 v232, v50
	v_exp_f32_e32 v233, v51
	v_exp_f32_e32 v234, v52
	v_exp_f32_e32 v235, v53
	v_pk_fma_f32 v[130:131], v[130:131], -0.5, -0.5 op_sel_hi:[1,0,0]
	v_pk_fma_f32 v[132:133], v[132:133], -0.5, -0.5 op_sel_hi:[1,0,0]
	v_pk_fma_f32 v[142:143], v[142:143], -0.5, -0.5 op_sel_hi:[1,0,0]
	v_pk_fma_f32 v[144:145], v[144:145], -0.5, -0.5 op_sel_hi:[1,0,0]
	v_pk_fma_f32 v[176:177], v[176:177], -0.5, -0.5 op_sel_hi:[1,0,0]
	v_pk_fma_f32 v[178:179], v[178:179], -0.5, -0.5 op_sel_hi:[1,0,0]
	v_pk_fma_f32 v[232:233], v[232:233], -0.5, -0.5 op_sel_hi:[1,0,0]
	v_pk_fma_f32 v[234:235], v[234:235], -0.5, -0.5 op_sel_hi:[1,0,0]
	v_pk_mul_f32 v[134:135], v[130:131], v[132:133]
	v_pk_mul_f32 v[146:147], v[142:143], v[144:145]
	v_pk_mul_f32 v[180:181], v[176:177], v[178:179]
	v_pk_mul_f32 v[236:237], v[232:233], v[234:235]
	v_mul_f32_e32 v138, v134, v135
	v_mul_f32_e32 v150, v146, v147
	v_mul_f32_e32 v184, v180, v181
	v_mul_f32_e32 v240, v236, v237
	v_rcp_f32_e32 v138, v138
	v_rcp_f32_e32 v150, v150
	v_rcp_f32_e32 v184, v184
	v_rcp_f32_e32 v240, v240
	v_pk_add_f32 v[164:165], v[164:165], v[86:87]
	v_pk_add_f32 v[164:165], v[164:165], v[88:89]
	v_pk_add_f32 v[164:165], v[164:165], v[38:39]
	v_pk_add_f32 v[164:165], v[164:165], v[40:41]
	v_pk_add_f32 v[164:165], v[164:165], v[122:123]
	v_pk_add_f32 v[164:165], v[164:165], v[124:125]
	v_pk_add_f32 v[164:165], v[164:165], v[50:51]
	v_pk_add_f32 v[164:165], v[164:165], v[52:53]
	v_pk_mul_f32 v[174:175], v[134:135], v[146:147]
	v_pk_mul_f32 v[174:175], v[174:175], v[180:181]
	v_pk_mul_f32 v[174:175], v[174:175], v[236:237]
	v_pk_mul_f32 v[136:137], v[138:139], v[134:135] op_sel:[0,1] op_sel_hi:[0,0]
	v_pk_mul_f32 v[148:149], v[150:151], v[146:147] op_sel:[0,1] op_sel_hi:[0,0]
	v_pk_mul_f32 v[182:183], v[184:185], v[180:181] op_sel:[0,1] op_sel_hi:[0,0]
	v_pk_mul_f32 v[238:239], v[240:241], v[236:237] op_sel:[0,1] op_sel_hi:[0,0]
	v_pk_fma_f32 v[138:139], v[136:137], v[132:133], 1.0 op_sel_hi:[1,1,0]
	v_pk_fma_f32 v[140:141], v[136:137], v[130:131], 1.0 op_sel_hi:[1,1,0]
	v_pk_fma_f32 v[150:151], v[148:149], v[144:145], 1.0 op_sel_hi:[1,1,0]
	v_pk_fma_f32 v[152:153], v[148:149], v[142:143], 1.0 op_sel_hi:[1,1,0]
	v_pk_fma_f32 v[184:185], v[182:183], v[178:179], 1.0 op_sel_hi:[1,1,0]
	v_pk_fma_f32 v[186:187], v[182:183], v[176:177], 1.0 op_sel_hi:[1,1,0]
	v_pk_fma_f32 v[240:241], v[238:239], v[234:235], 1.0 op_sel_hi:[1,1,0]
	v_pk_fma_f32 v[242:243], v[238:239], v[232:233], 1.0 op_sel_hi:[1,1,0]
	v_cvt_pk_bf16_f32 v154, v138, v139
	v_cvt_pk_bf16_f32 v155, v140, v141
	v_cvt_pk_bf16_f32 v156, v150, v151
	v_cvt_pk_bf16_f32 v157, v152, v153
	v_cvt_pk_bf16_f32 v158, v184, v185
	v_cvt_pk_bf16_f32 v159, v186, v187
	v_cvt_pk_bf16_f32 v160, v240, v241
	v_cvt_pk_bf16_f32 v161, v242, v243
	ds_read_b128 v[86:89], v172 offset:512
	ds_read_b128 v[38:41], v172 offset:576
	ds_read_b128 v[122:125], v172 offset:640
	ds_read_b128 v[50:53], v172 offset:704
	v_permlane16_swap_b32_e32 v154, v156
	v_permlane16_swap_b32_e32 v155, v157
	global_store_dwordx4 v228, v[154:157], s[62:63] offset:2048 nt
	v_permlane16_swap_b32_e32 v158, v160
	v_permlane16_swap_b32_e32 v159, v161
	global_store_dwordx4 v228, v[158:161], s[62:63] offset:2176 nt
	v_log_f32_e32 v166, v162
	v_log_f32_e32 v167, v163
	v_log_f32_e32 v170, v174
	v_log_f32_e32 v171, v175
	v_add_f32_e32 v168, v164, v165
	v_mul_f32_e32 v168, 0xbeb17218, v168
	v_add_f32_e32 v166, v166, v167
	v_add_f32_e32 v170, v170, v171
	v_add_f32_e32 v166, v166, v170
	v_fmac_f32_e32 v168, 0x3f317218, v166
	v_mov_b32_e32 v169, v168
	s_nop 1
	v_permlane16_swap_b32_e32 v168, v169
	v_add_f32_e32 v168, v168, v169
	v_mov_b32_e32 v169, v168
	s_nop 1
	v_permlane32_swap_b32_e32 v168, v169
	v_add_f32_e32 v168, v168, v169
	s_mov_b64 exec, s[0:1]
	global_store_dword v229, v168, s[66:67] offset:64
	s_mov_b64 exec, -1
	v_exp_f32_e32 v130, v98
	v_exp_f32_e32 v131, v99
	v_exp_f32_e32 v132, v100
	v_exp_f32_e32 v133, v101
	v_exp_f32_e32 v142, v62
	v_exp_f32_e32 v143, v63
	v_exp_f32_e32 v144, v64
	v_exp_f32_e32 v145, v65
	v_exp_f32_e32 v176, v94
	v_exp_f32_e32 v177, v95
	v_exp_f32_e32 v178, v96
	v_exp_f32_e32 v179, v97
	v_exp_f32_e32 v232, v54
	v_exp_f32_e32 v233, v55
	v_exp_f32_e32 v234, v56
	v_exp_f32_e32 v235, v57
	v_pk_fma_f32 v[130:131], v[130:131], -0.5, -0.5 op_sel_hi:[1,0,0]
	v_pk_fma_f32 v[132:133], v[132:133], -0.5, -0.5 op_sel_hi:[1,0,0]
	v_pk_fma_f32 v[142:143], v[142:143], -0.5, -0.5 op_sel_hi:[1,0,0]
	v_pk_fma_f32 v[144:145], v[144:145], -0.5, -0.5 op_sel_hi:[1,0,0]
	v_pk_fma_f32 v[176:177], v[176:177], -0.5, -0.5 op_sel_hi:[1,0,0]
	v_pk_fma_f32 v[178:179], v[178:179], -0.5, -0.5 op_sel_hi:[1,0,0]
	v_pk_fma_f32 v[232:233], v[232:233], -0.5, -0.5 op_sel_hi:[1,0,0]
	v_pk_fma_f32 v[234:235], v[234:235], -0.5, -0.5 op_sel_hi:[1,0,0]
	v_pk_mul_f32 v[134:135], v[130:131], v[132:133]
	v_pk_mul_f32 v[146:147], v[142:143], v[144:145]
	v_pk_mul_f32 v[180:181], v[176:177], v[178:179]
	v_pk_mul_f32 v[236:237], v[232:233], v[234:235]
	v_mul_f32_e32 v138, v134, v135
	v_mul_f32_e32 v150, v146, v147
	v_mul_f32_e32 v184, v180, v181
	v_mul_f32_e32 v240, v236, v237
	v_rcp_f32_e32 v138, v138
	v_rcp_f32_e32 v150, v150
	v_rcp_f32_e32 v184, v184
	v_rcp_f32_e32 v240, v240
	v_pk_add_f32 v[164:165], v[98:99], v[100:101]
	v_pk_add_f32 v[164:165], v[164:165], v[62:63]
	v_pk_add_f32 v[164:165], v[164:165], v[64:65]
	v_pk_add_f32 v[164:165], v[164:165], v[94:95]
	v_pk_add_f32 v[164:165], v[164:165], v[96:97]
	v_pk_add_f32 v[164:165], v[164:165], v[54:55]
	v_pk_add_f32 v[164:165], v[164:165], v[56:57]
	v_pk_mul_f32 v[162:163], v[134:135], v[146:147]
	v_pk_mul_f32 v[162:163], v[162:163], v[180:181]
	v_pk_mul_f32 v[162:163], v[162:163], v[236:237]
	v_pk_mul_f32 v[136:137], v[138:139], v[134:135] op_sel:[0,1] op_sel_hi:[0,0]
	v_pk_mul_f32 v[148:149], v[150:151], v[146:147] op_sel:[0,1] op_sel_hi:[0,0]
	v_pk_mul_f32 v[182:183], v[184:185], v[180:181] op_sel:[0,1] op_sel_hi:[0,0]
	v_pk_mul_f32 v[238:239], v[240:241], v[236:237] op_sel:[0,1] op_sel_hi:[0,0]
	v_pk_fma_f32 v[138:139], v[136:137], v[132:133], 1.0 op_sel_hi:[1,1,0]
	v_pk_fma_f32 v[140:141], v[136:137], v[130:131], 1.0 op_sel_hi:[1,1,0]
	v_pk_fma_f32 v[150:151], v[148:149], v[144:145], 1.0 op_sel_hi:[1,1,0]
	v_pk_fma_f32 v[152:153], v[148:149], v[142:143], 1.0 op_sel_hi:[1,1,0]
	v_pk_fma_f32 v[184:185], v[182:183], v[178:179], 1.0 op_sel_hi:[1,1,0]
	v_pk_fma_f32 v[186:187], v[182:183], v[176:177], 1.0 op_sel_hi:[1,1,0]
	v_pk_fma_f32 v[240:241], v[238:239], v[234:235], 1.0 op_sel_hi:[1,1,0]
	v_pk_fma_f32 v[242:243], v[238:239], v[232:233], 1.0 op_sel_hi:[1,1,0]
	v_cvt_pk_bf16_f32 v154, v138, v139
	v_cvt_pk_bf16_f32 v155, v140, v141
	v_cvt_pk_bf16_f32 v156, v150, v151
	v_cvt_pk_bf16_f32 v157, v152, v153
	v_cvt_pk_bf16_f32 v158, v184, v185
	v_cvt_pk_bf16_f32 v159, v186, v187
	v_cvt_pk_bf16_f32 v160, v240, v241
	v_cvt_pk_bf16_f32 v161, v242, v243
	ds_read_b128 v[98:101], v172
	ds_read_b128 v[62:65], v172 offset:64
	ds_read_b128 v[94:97], v172 offset:128
	ds_read_b128 v[54:57], v172 offset:192
	v_permlane16_swap_b32_e32 v154, v156
	v_permlane16_swap_b32_e32 v155, v157
	global_store_dwordx4 v228, v[154:157], s[60:61] nt
	v_permlane16_swap_b32_e32 v158, v160
	v_permlane16_swap_b32_e32 v159, v161
	global_store_dwordx4 v228, v[158:161], s[60:61] offset:128 nt
	v_exp_f32_e32 v130, v82
	v_exp_f32_e32 v131, v83
	v_exp_f32_e32 v132, v84
	v_exp_f32_e32 v133, v85
	v_exp_f32_e32 v142, v34
	v_exp_f32_e32 v143, v35
	v_exp_f32_e32 v144, v36
	v_exp_f32_e32 v145, v37
	v_exp_f32_e32 v176, v118
	v_exp_f32_e32 v177, v119
	v_exp_f32_e32 v178, v120
	v_exp_f32_e32 v179, v121
	v_exp_f32_e32 v232, v46
	v_exp_f32_e32 v233, v47
	v_exp_f32_e32 v234, v48
	v_exp_f32_e32 v235, v49
	v_pk_fma_f32 v[130:131], v[130:131], -0.5, -0.5 op_sel_hi:[1,0,0]
	v_pk_fma_f32 v[132:133], v[132:133], -0.5, -0.5 op_sel_hi:[1,0,0]
	v_pk_fma_f32 v[142:143], v[142:143], -0.5, -0.5 op_sel_hi:[1,0,0]
	v_pk_fma_f32 v[144:145], v[144:145], -0.5, -0.5 op_sel_hi:[1,0,0]
	v_pk_fma_f32 v[176:177], v[176:177], -0.5, -0.5 op_sel_hi:[1,0,0]
	v_pk_fma_f32 v[178:179], v[178:179], -0.5, -0.5 op_sel_hi:[1,0,0]
	v_pk_fma_f32 v[232:233], v[232:233], -0.5, -0.5 op_sel_hi:[1,0,0]
	v_pk_fma_f32 v[234:235], v[234:235], -0.5, -0.5 op_sel_hi:[1,0,0]
	v_pk_mul_f32 v[134:135], v[130:131], v[132:133]
	v_pk_mul_f32 v[146:147], v[142:143], v[144:145]
	v_pk_mul_f32 v[180:181], v[176:177], v[178:179]
	v_pk_mul_f32 v[236:237], v[232:233], v[234:235]
	v_mul_f32_e32 v138, v134, v135
	v_mul_f32_e32 v150, v146, v147
	v_mul_f32_e32 v184, v180, v181
	v_mul_f32_e32 v240, v236, v237
	v_rcp_f32_e32 v138, v138
	v_rcp_f32_e32 v150, v150
	v_rcp_f32_e32 v184, v184
	v_rcp_f32_e32 v240, v240
	v_pk_add_f32 v[164:165], v[164:165], v[82:83]
	v_pk_add_f32 v[164:165], v[164:165], v[84:85]
	v_pk_add_f32 v[164:165], v[164:165], v[34:35]
	v_pk_add_f32 v[164:165], v[164:165], v[36:37]
	v_pk_add_f32 v[164:165], v[164:165], v[118:119]
	v_pk_add_f32 v[164:165], v[164:165], v[120:121]
	v_pk_add_f32 v[164:165], v[164:165], v[46:47]
	v_pk_add_f32 v[164:165], v[164:165], v[48:49]
	v_pk_mul_f32 v[174:175], v[134:135], v[146:147]
	v_pk_mul_f32 v[174:175], v[174:175], v[180:181]
	v_pk_mul_f32 v[174:175], v[174:175], v[236:237]
	v_pk_mul_f32 v[136:137], v[138:139], v[134:135] op_sel:[0,1] op_sel_hi:[0,0]
	v_pk_mul_f32 v[148:149], v[150:151], v[146:147] op_sel:[0,1] op_sel_hi:[0,0]
	v_pk_mul_f32 v[182:183], v[184:185], v[180:181] op_sel:[0,1] op_sel_hi:[0,0]
	v_pk_mul_f32 v[238:239], v[240:241], v[236:237] op_sel:[0,1] op_sel_hi:[0,0]
	v_pk_fma_f32 v[138:139], v[136:137], v[132:133], 1.0 op_sel_hi:[1,1,0]
	v_pk_fma_f32 v[140:141], v[136:137], v[130:131], 1.0 op_sel_hi:[1,1,0]
	v_pk_fma_f32 v[150:151], v[148:149], v[144:145], 1.0 op_sel_hi:[1,1,0]
	v_pk_fma_f32 v[152:153], v[148:149], v[142:143], 1.0 op_sel_hi:[1,1,0]
	v_pk_fma_f32 v[184:185], v[182:183], v[178:179], 1.0 op_sel_hi:[1,1,0]
	v_pk_fma_f32 v[186:187], v[182:183], v[176:177], 1.0 op_sel_hi:[1,1,0]
	v_pk_fma_f32 v[240:241], v[238:239], v[234:235], 1.0 op_sel_hi:[1,1,0]
	v_pk_fma_f32 v[242:243], v[238:239], v[232:233], 1.0 op_sel_hi:[1,1,0]
	v_cvt_pk_bf16_f32 v154, v138, v139
	v_cvt_pk_bf16_f32 v155, v140, v141
	v_cvt_pk_bf16_f32 v156, v150, v151
	v_cvt_pk_bf16_f32 v157, v152, v153
	v_cvt_pk_bf16_f32 v158, v184, v185
	v_cvt_pk_bf16_f32 v159, v186, v187
	v_cvt_pk_bf16_f32 v160, v240, v241
	v_cvt_pk_bf16_f32 v161, v242, v243
	ds_read_b128 v[82:85], v172 offset:512
	ds_read_b128 v[34:37], v172 offset:576
	ds_read_b128 v[118:121], v172 offset:640
	ds_read_b128 v[46:49], v172 offset:704
	v_permlane16_swap_b32_e32 v154, v156
	v_permlane16_swap_b32_e32 v155, v157
	global_store_dwordx4 v228, v[154:157], s[64:65] nt
	v_permlane16_swap_b32_e32 v158, v160
	v_permlane16_swap_b32_e32 v159, v161
	global_store_dwordx4 v228, v[158:161], s[64:65] offset:128 nt
	v_log_f32_e32 v166, v162
	v_log_f32_e32 v167, v163
	v_log_f32_e32 v170, v174
	v_log_f32_e32 v171, v175
	v_add_f32_e32 v168, v164, v165
	v_mul_f32_e32 v168, 0xbeb17218, v168
	v_add_f32_e32 v166, v166, v167
	v_add_f32_e32 v170, v170, v171
	v_add_f32_e32 v166, v166, v170
	v_fmac_f32_e32 v168, 0x3f317218, v166
	v_mov_b32_e32 v169, v168
	s_nop 1
	v_permlane16_swap_b32_e32 v168, v169
	v_add_f32_e32 v168, v168, v169
	v_mov_b32_e32 v169, v168
	s_nop 1
	v_permlane32_swap_b32_e32 v168, v169
	v_add_f32_e32 v168, v168, v169
	s_mov_b64 exec, s[0:1]
	global_store_dword v229, v168, s[66:67] offset:512
	s_mov_b64 exec, -1
	s_bitcmp1_b32 s20, 12
	s_cbranch_scc0 .Lg1_noY
	s_barrier
.Lg1_noY:
	v_exp_f32_e32 v130, v18
	v_exp_f32_e32 v131, v19
	v_exp_f32_e32 v132, v20
	v_exp_f32_e32 v133, v21
	v_exp_f32_e32 v142, v2
	v_exp_f32_e32 v143, v3
	v_exp_f32_e32 v144, v4
	v_exp_f32_e32 v145, v5
	v_exp_f32_e32 v176, v26
	v_exp_f32_e32 v177, v27
	v_exp_f32_e32 v178, v28
	v_exp_f32_e32 v179, v29
	v_exp_f32_e32 v232, v10
	v_exp_f32_e32 v233, v11
	v_exp_f32_e32 v234, v12
	v_exp_f32_e32 v235, v13
	v_pk_fma_f32 v[130:131], v[130:131], -0.5, -0.5 op_sel_hi:[1,0,0]
	v_pk_fma_f32 v[132:133], v[132:133], -0.5, -0.5 op_sel_hi:[1,0,0]
	v_pk_fma_f32 v[142:143], v[142:143], -0.5, -0.5 op_sel_hi:[1,0,0]
	v_pk_fma_f32 v[144:145], v[144:145], -0.5, -0.5 op_sel_hi:[1,0,0]
	v_pk_fma_f32 v[176:177], v[176:177], -0.5, -0.5 op_sel_hi:[1,0,0]
	v_pk_fma_f32 v[178:179], v[178:179], -0.5, -0.5 op_sel_hi:[1,0,0]
	v_pk_fma_f32 v[232:233], v[232:233], -0.5, -0.5 op_sel_hi:[1,0,0]
	v_pk_fma_f32 v[234:235], v[234:235], -0.5, -0.5 op_sel_hi:[1,0,0]
	v_pk_mul_f32 v[134:135], v[130:131], v[132:133]
	v_pk_mul_f32 v[146:147], v[142:143], v[144:145]
	v_pk_mul_f32 v[180:181], v[176:177], v[178:179]
	v_pk_mul_f32 v[236:237], v[232:233], v[234:235]
	v_mul_f32_e32 v138, v134, v135
	v_mul_f32_e32 v150, v146, v147
	v_mul_f32_e32 v184, v180, v181
	v_mul_f32_e32 v240, v236, v237
	v_rcp_f32_e32 v138, v138
	v_rcp_f32_e32 v150, v150
	v_rcp_f32_e32 v184, v184
	v_rcp_f32_e32 v240, v240
	v_pk_add_f32 v[164:165], v[18:19], v[20:21]
	v_pk_add_f32 v[164:165], v[164:165], v[2:3]
	v_pk_add_f32 v[164:165], v[164:165], v[4:5]
	v_pk_add_f32 v[164:165], v[164:165], v[26:27]
	v_pk_add_f32 v[164:165], v[164:165], v[28:29]
	v_pk_add_f32 v[164:165], v[164:165], v[10:11]
	v_pk_add_f32 v[164:165], v[164:165], v[12:13]
	v_pk_mul_f32 v[162:163], v[134:135], v[146:147]
	v_pk_mul_f32 v[162:163], v[162:163], v[180:181]
	v_pk_mul_f32 v[162:163], v[162:163], v[236:237]
	v_pk_mul_f32 v[136:137], v[138:139], v[134:135] op_sel:[0,1] op_sel_hi:[0,0]
	v_pk_mul_f32 v[148:149], v[150:151], v[146:147] op_sel:[0,1] op_sel_hi:[0,0]
	v_pk_mul_f32 v[182:183], v[184:185], v[180:181] op_sel:[0,1] op_sel_hi:[0,0]
	v_pk_mul_f32 v[238:239], v[240:241], v[236:237] op_sel:[0,1] op_sel_hi:[0,0]
	v_pk_fma_f32 v[138:139], v[136:137], v[132:133], 1.0 op_sel_hi:[1,1,0]
	v_pk_fma_f32 v[140:141], v[136:137], v[130:131], 1.0 op_sel_hi:[1,1,0]
	v_pk_fma_f32 v[150:151], v[148:149], v[144:145], 1.0 op_sel_hi:[1,1,0]
	v_pk_fma_f32 v[152:153], v[148:149], v[142:143], 1.0 op_sel_hi:[1,1,0]
	v_pk_fma_f32 v[184:185], v[182:183], v[178:179], 1.0 op_sel_hi:[1,1,0]
	v_pk_fma_f32 v[186:187], v[182:183], v[176:177], 1.0 op_sel_hi:[1,1,0]
	v_pk_fma_f32 v[240:241], v[238:239], v[234:235], 1.0 op_sel_hi:[1,1,0]
	v_pk_fma_f32 v[242:243], v[238:239], v[232:233], 1.0 op_sel_hi:[1,1,0]
	v_cvt_pk_bf16_f32 v154, v138, v139
	v_cvt_pk_bf16_f32 v155, v140, v141
	v_cvt_pk_bf16_f32 v156, v150, v151
	v_cvt_pk_bf16_f32 v157, v152, v153
	v_cvt_pk_bf16_f32 v158, v184, v185
	v_cvt_pk_bf16_f32 v159, v186, v187
	v_cvt_pk_bf16_f32 v160, v240, v241
	v_cvt_pk_bf16_f32 v161, v242, v243
	ds_read_b128 v[18:21], v172
	ds_read_b128 v[2:5], v172 offset:64
	ds_read_b128 v[26:29], v172 offset:128
	ds_read_b128 v[10:13], v172 offset:192
	v_permlane16_swap_b32_e32 v154, v156
	v_permlane16_swap_b32_e32 v155, v157
	global_store_dwordx4 v228, v[154:157], s[60:61] offset:2048 nt
	v_permlane16_swap_b32_e32 v158, v160
	v_permlane16_swap_b32_e32 v159, v161
	global_store_dwordx4 v228, v[158:161], s[60:61] offset:2176 nt
	v_exp_f32_e32 v130, v22
	v_exp_f32_e32 v131, v23
	v_exp_f32_e32 v132, v24
	v_exp_f32_e32 v133, v25
	v_exp_f32_e32 v142, v6
	v_exp_f32_e32 v143, v7
	v_exp_f32_e32 v144, v8
	v_exp_f32_e32 v145, v9
	v_exp_f32_e32 v176, v30
	v_exp_f32_e32 v177, v31
	v_exp_f32_e32 v178, v32
	v_exp_f32_e32 v179, v33
	v_exp_f32_e32 v232, v14
	v_exp_f32_e32 v233, v15
	v_exp_f32_e32 v234, v16
	v_exp_f32_e32 v235, v17
	v_pk_fma_f32 v[130:131], v[130:131], -0.5, -0.5 op_sel_hi:[1,0,0]
	v_pk_fma_f32 v[132:133], v[132:133], -0.5, -0.5 op_sel_hi:[1,0,0]
	v_pk_fma_f32 v[142:143], v[142:143], -0.5, -0.5 op_sel_hi:[1,0,0]
	v_pk_fma_f32 v[144:145], v[144:145], -0.5, -0.5 op_sel_hi:[1,0,0]
	v_pk_fma_f32 v[176:177], v[176:177], -0.5, -0.5 op_sel_hi:[1,0,0]
	v_pk_fma_f32 v[178:179], v[178:179], -0.5, -0.5 op_sel_hi:[1,0,0]
	v_pk_fma_f32 v[232:233], v[232:233], -0.5, -0.5 op_sel_hi:[1,0,0]
	v_pk_fma_f32 v[234:235], v[234:235], -0.5, -0.5 op_sel_hi:[1,0,0]
	v_pk_mul_f32 v[134:135], v[130:131], v[132:133]
	v_pk_mul_f32 v[146:147], v[142:143], v[144:145]
	v_pk_mul_f32 v[180:181], v[176:177], v[178:179]
	v_pk_mul_f32 v[236:237], v[232:233], v[234:235]
	v_mul_f32_e32 v138, v134, v135
	v_mul_f32_e32 v150, v146, v147
	v_mul_f32_e32 v184, v180, v181
	v_mul_f32_e32 v240, v236, v237
	v_rcp_f32_e32 v138, v138
	v_rcp_f32_e32 v150, v150
	v_rcp_f32_e32 v184, v184
	v_rcp_f32_e32 v240, v240
	v_pk_add_f32 v[164:165], v[164:165], v[22:23]
	v_pk_add_f32 v[164:165], v[164:165], v[24:25]
	v_pk_add_f32 v[164:165], v[164:165], v[6:7]
	v_pk_add_f32 v[164:165], v[164:165], v[8:9]
	v_pk_add_f32 v[164:165], v[164:165], v[30:31]
	v_pk_add_f32 v[164:165], v[164:165], v[32:33]
	v_pk_add_f32 v[164:165], v[164:165], v[14:15]
	v_pk_add_f32 v[164:165], v[164:165], v[16:17]
	v_pk_mul_f32 v[174:175], v[134:135], v[146:147]
	v_pk_mul_f32 v[174:175], v[174:175], v[180:181]
	v_pk_mul_f32 v[174:175], v[174:175], v[236:237]
	v_pk_mul_f32 v[136:137], v[138:139], v[134:135] op_sel:[0,1] op_sel_hi:[0,0]
	v_pk_mul_f32 v[148:149], v[150:151], v[146:147] op_sel:[0,1] op_sel_hi:[0,0]
	v_pk_mul_f32 v[182:183], v[184:185], v[180:181] op_sel:[0,1] op_sel_hi:[0,0]
	v_pk_mul_f32 v[238:239], v[240:241], v[236:237] op_sel:[0,1] op_sel_hi:[0,0]
	v_pk_fma_f32 v[138:139], v[136:137], v[132:133], 1.0 op_sel_hi:[1,1,0]
	v_pk_fma_f32 v[140:141], v[136:137], v[130:131], 1.0 op_sel_hi:[1,1,0]
	v_pk_fma_f32 v[150:151], v[148:149], v[144:145], 1.0 op_sel_hi:[1,1,0]
	v_pk_fma_f32 v[152:153], v[148:149], v[142:143], 1.0 op_sel_hi:[1,1,0]
	v_pk_fma_f32 v[184:185], v[182:183], v[178:179], 1.0 op_sel_hi:[1,1,0]
	v_pk_fma_f32 v[186:187], v[182:183], v[176:177], 1.0 op_sel_hi:[1,1,0]
	v_pk_fma_f32 v[240:241], v[238:239], v[234:235], 1.0 op_sel_hi:[1,1,0]
	v_pk_fma_f32 v[242:243], v[238:239], v[232:233], 1.0 op_sel_hi:[1,1,0]
	v_cvt_pk_bf16_f32 v154, v138, v139
	v_cvt_pk_bf16_f32 v155, v140, v141
	v_cvt_pk_bf16_f32 v156, v150, v151
	v_cvt_pk_bf16_f32 v157, v152, v153
	v_cvt_pk_bf16_f32 v158, v184, v185
	v_cvt_pk_bf16_f32 v159, v186, v187
	v_cvt_pk_bf16_f32 v160, v240, v241
	v_cvt_pk_bf16_f32 v161, v242, v243
	ds_read_b128 v[22:25], v172 offset:512
	ds_read_b128 v[6:9], v172 offset:576
	ds_read_b128 v[30:33], v172 offset:640
	ds_read_b128 v[14:17], v172 offset:704
	v_permlane16_swap_b32_e32 v154, v156
	v_permlane16_swap_b32_e32 v155, v157
	global_store_dwordx4 v228, v[154:157], s[64:65] offset:2048 nt
	v_permlane16_swap_b32_e32 v158, v160
	v_permlane16_swap_b32_e32 v159, v161
	global_store_dwordx4 v228, v[158:161], s[64:65] offset:2176 nt
	v_log_f32_e32 v166, v162
	v_log_f32_e32 v167, v163
	v_log_f32_e32 v170, v174
	v_log_f32_e32 v171, v175
	v_add_f32_e32 v168, v164, v165
	v_mul_f32_e32 v168, 0xbeb17218, v168
	v_add_f32_e32 v166, v166, v167
	v_add_f32_e32 v170, v170, v171
	v_add_f32_e32 v166, v166, v170
	v_fmac_f32_e32 v168, 0x3f317218, v166
	v_mov_b32_e32 v169, v168
	s_nop 1
	v_permlane16_swap_b32_e32 v168, v169
	v_add_f32_e32 v168, v168, v169
	v_mov_b32_e32 v169, v168
	s_nop 1
	v_permlane32_swap_b32_e32 v168, v169
	v_add_f32_e32 v168, v168, v169
	s_mov_b64 exec, s[0:1]
	global_store_dword v229, v168, s[66:67] offset:576
	s_mov_b64 exec, -1
	s_mov_b64 s[2:3], 0
	s_branch .LBB3_5
